# P11 and P4: the two wave halves keep their one-barrier stagger through the epilogue (each half's epilogue overlaps the other half's MFMA segment) instead of re-aligning at every unit
# speedup vs baseline: 1.0053x; 1.0043x over previous
.LBB0_757:
	s_andn2_b64 vcc, s[10:11], s[4:5]
	s_cbranch_vccz .LBB0_759
	s_barrier
.LBB0_759:
	s_lshl_b32 s15, s57, 11
	v_mov_b32_e32 v196, v198
	s_and_b32 s15, s15, 0x800
	s_add_i32 s15, s52, s15
	v_and_b32_e32 v210, 15, v196
	v_lshl_add_u32 v211, v210, 3, s15
	ds_read2_b64 v[192:195], v211 offset1:16
	v_ashrrev_i32_e32 v214, 1, v196
	s_lshl_b32 s15, s22, 8
	s_add_i32 s15, s15, s50
	v_or_b32_e32 v210, s15, v210
	s_waitcnt lgkmcnt(0)
	v_mov_b32_e32 v196, v193
	v_lshlrev_b64 v[212:213], s54, v[196:197]
	v_min_u32_e32 v193, 1, v212
	v_or_b32_e32 v193, v213, v193
	v_cvt_f32_u32_e32 v193, v193
	v_cvt_f32_u32_e32 v192, v192
	s_sub_i32 s15, 32, s54
	v_mov_b32_e32 v196, v195
	v_ldexp_f32 v193, v193, s15
	v_fmamk_f32 v212, v192, 0x2e000000, v209
	v_fmac_f32_e32 v212, 0x3e000000, v193
	v_lshlrev_b64 v[192:193], s54, v[196:197]
	v_min_u32_e32 v192, 1, v192
	v_or_b32_e32 v192, v193, v192
	v_cvt_f32_u32_e32 v196, v192
	v_cvt_f32_u32_e32 v213, v194
	ds_read2_b64 v[192:195], v211 offset0:32 offset1:48
	v_rsq_f32_e32 v215, v212
	v_ldexp_f32 v196, v196, s15
	v_fmamk_f32 v212, v213, 0x2e000000, v209
	v_fmac_f32_e32 v212, 0x3e000000, v196
	s_waitcnt lgkmcnt(0)
	v_mov_b32_e32 v196, v193
	v_rsq_f32_e32 v216, v212
	v_lshlrev_b64 v[212:213], s54, v[196:197]
	v_min_u32_e32 v193, 1, v212
	v_or_b32_e32 v193, v213, v193
	v_cvt_f32_u32_e32 v193, v193
	v_cvt_f32_u32_e32 v192, v192
	v_mov_b32_e32 v196, v195
	v_cvt_f32_u32_e32 v213, v194
	v_ldexp_f32 v193, v193, s15
	v_fmamk_f32 v212, v192, 0x2e000000, v209
	v_fmac_f32_e32 v212, 0x3e000000, v193
	v_lshlrev_b64 v[192:193], s54, v[196:197]
	v_min_u32_e32 v192, 1, v192
	v_or_b32_e32 v192, v193, v192
	v_cvt_f32_u32_e32 v196, v192
	ds_read2_b64 v[192:195], v211 offset0:128 offset1:144
	v_rsq_f32_e32 v217, v212
	v_fmamk_f32 v212, v213, 0x2e000000, v209
	v_ldexp_f32 v196, v196, s15
	v_fmac_f32_e32 v212, 0x3e000000, v196
	s_waitcnt lgkmcnt(0)
	v_mov_b32_e32 v196, v193
	v_rsq_f32_e32 v218, v212
	v_lshlrev_b64 v[212:213], s54, v[196:197]
	v_min_u32_e32 v193, 1, v212
	v_or_b32_e32 v193, v213, v193
	v_cvt_f32_u32_e32 v193, v193
	v_cvt_f32_u32_e32 v192, v192
	v_mov_b32_e32 v196, v195
	v_cvt_f32_u32_e32 v219, v194
	v_ldexp_f32 v212, v193, s15
	v_fmamk_f32 v213, v192, 0x2e000000, v209
	v_lshlrev_b64 v[192:193], s54, v[196:197]
	v_min_u32_e32 v192, 1, v192
	v_or_b32_e32 v192, v193, v192
	v_cvt_f32_u32_e32 v196, v192
	ds_read2_b64 v[192:195], v211 offset0:160 offset1:176
	v_fmac_f32_e32 v213, 0x3e000000, v212
	v_rsq_f32_e32 v211, v213
	v_ldexp_f32 v220, v196, s15
	v_fmamk_f32 v219, v219, 0x2e000000, v209
	s_waitcnt lgkmcnt(0)
	v_mov_b32_e32 v196, v193
	v_lshlrev_b64 v[212:213], s54, v[196:197]
	v_min_u32_e32 v193, 1, v212
	v_or_b32_e32 v193, v213, v193
	v_cvt_f32_u32_e32 v193, v193
	v_cvt_f32_u32_e32 v192, v192
	v_fmac_f32_e32 v219, 0x3e000000, v220
	v_mov_b32_e32 v196, v195
	v_rsq_f32_e32 v212, v219
	v_ldexp_f32 v213, v193, s15
	v_fmamk_f32 v219, v192, 0x2e000000, v209
	v_lshlrev_b64 v[192:193], s54, v[196:197]
	v_min_u32_e32 v192, 1, v192
	v_or_b32_e32 v192, v193, v192
	v_cvt_f32_u32_e32 v192, v192
	v_cvt_f32_u32_e32 v193, v194
	v_fmac_f32_e32 v219, 0x3e000000, v213
	v_rsq_f32_e32 v194, v219
	v_ldexp_f32 v192, v192, s15
	v_fmamk_f32 v193, v193, 0x2e000000, v209
	v_fmac_f32_e32 v193, 0x3e000000, v192
	v_rsq_f32_e32 v192, v193
	v_mul_f32_e32 v224, 0x37d834f1, v215
	v_mul_f32_e32 v225, 0x37d834f1, v216
	v_mul_f32_e32 v226, 0x37d834f1, v217
	v_mul_f32_e32 v227, 0x37d834f1, v218
	v_mul_f32_e32 v228, 0x37d834f1, v211
	v_mul_f32_e32 v229, 0x37d834f1, v212
	v_mul_f32_e32 v230, 0x37d834f1, v194
	v_mul_f32_e32 v231, 0x37d834f1, v192
	s_lshl_b32 s15, s56, 7
	v_and_b32_e32 v214, -8, v214
	s_or_b32 s15, s15, s51
	v_add_u32_e32 v214, s15, v214
	v_lshlrev_b32_e32 v214, 1, v214
	v_mad_u32_u24 v232, v210, s53, v214
	v_mul_f32_e32 v78, 0xbfb8aa3b, v224
	v_mul_f32_e32 v20, v224, v224
	v_rcp_f32_e32 v20, v20
	v_cvt_f32_i32_e32 v184, v184
	v_cvt_f32_i32_e32 v185, v185
	v_cvt_f32_i32_e32 v186, v186
	v_cvt_f32_i32_e32 v187, v187
	v_cvt_f32_i32_e32 v176, v176
	v_cvt_f32_i32_e32 v177, v177
	v_cvt_f32_i32_e32 v178, v178
	v_cvt_f32_i32_e32 v179, v179
	v_cvt_f32_i32_e32 v188, v188
	v_cvt_f32_i32_e32 v189, v189
	v_cvt_f32_i32_e32 v190, v190
	v_cvt_f32_i32_e32 v191, v191
	v_cvt_f32_i32_e32 v180, v180
	v_cvt_f32_i32_e32 v181, v181
	v_cvt_f32_i32_e32 v182, v182
	v_cvt_f32_i32_e32 v183, v183
	v_pk_mul_f32 v[64:65], v[184:185], v[78:79] op_sel_hi:[1,0]
	v_pk_mul_f32 v[66:67], v[186:187], v[78:79] op_sel_hi:[1,0]
	v_pk_mul_f32 v[68:69], v[176:177], v[78:79] op_sel_hi:[1,0]
	v_pk_mul_f32 v[70:71], v[178:179], v[78:79] op_sel_hi:[1,0]
	v_exp_f32_e32 v64, v64
	v_exp_f32_e32 v65, v65
	v_exp_f32_e32 v66, v66
	v_exp_f32_e32 v67, v67
	v_exp_f32_e32 v68, v68
	v_exp_f32_e32 v69, v69
	v_exp_f32_e32 v70, v70
	v_exp_f32_e32 v71, v71
	v_pk_mul_f32 v[184:185], v[188:189], v[184:185]
	v_pk_mul_f32 v[186:187], v[190:191], v[186:187]
	v_pk_mul_f32 v[176:177], v[180:181], v[176:177]
	v_pk_mul_f32 v[178:179], v[182:183], v[178:179]
	v_pk_fma_f32 v[64:65], v[64:65], v[20:21], v[20:21] op_sel_hi:[1,0,0]
	v_pk_fma_f32 v[66:67], v[66:67], v[20:21], v[20:21] op_sel_hi:[1,0,0]
	v_pk_fma_f32 v[68:69], v[68:69], v[20:21], v[20:21] op_sel_hi:[1,0,0]
	v_pk_fma_f32 v[70:71], v[70:71], v[20:21], v[20:21] op_sel_hi:[1,0,0]
	v_rcp_f32_e32 v64, v64
	v_rcp_f32_e32 v65, v65
	v_rcp_f32_e32 v66, v66
	v_rcp_f32_e32 v67, v67
	v_rcp_f32_e32 v68, v68
	v_rcp_f32_e32 v69, v69
	v_rcp_f32_e32 v70, v70
	v_rcp_f32_e32 v71, v71
	v_mov_b32_e32 v76, v232
	v_pk_mul_f32 v[184:185], v[184:185], v[64:65]
	v_pk_mul_f32 v[186:187], v[186:187], v[66:67]
	v_pk_mul_f32 v[176:177], v[176:177], v[68:69]
	v_pk_mul_f32 v[178:179], v[178:179], v[70:71]
	v_cvt_pk_bf16_f32 v72, v184, v185
	v_cvt_pk_bf16_f32 v73, v186, v187
	v_cvt_pk_bf16_f32 v74, v176, v177
	v_cvt_pk_bf16_f32 v75, v178, v179
	global_store_dwordx4 v76, v[72:75], s[8:9]
	v_mul_f32_e32 v94, 0xbfb8aa3b, v225
	v_mul_f32_e32 v24, v225, v225
	v_rcp_f32_e32 v24, v24
	v_cvt_f32_i32_e32 v168, v168
	v_cvt_f32_i32_e32 v169, v169
	v_cvt_f32_i32_e32 v170, v170
	v_cvt_f32_i32_e32 v171, v171
	v_cvt_f32_i32_e32 v160, v160
	v_cvt_f32_i32_e32 v161, v161
	v_cvt_f32_i32_e32 v162, v162
	v_cvt_f32_i32_e32 v163, v163
	v_cvt_f32_i32_e32 v172, v172
	v_cvt_f32_i32_e32 v173, v173
	v_cvt_f32_i32_e32 v174, v174
	v_cvt_f32_i32_e32 v175, v175
	v_cvt_f32_i32_e32 v164, v164
	v_cvt_f32_i32_e32 v165, v165
	v_cvt_f32_i32_e32 v166, v166
	v_cvt_f32_i32_e32 v167, v167
	v_pk_mul_f32 v[80:81], v[168:169], v[94:95] op_sel_hi:[1,0]
	v_pk_mul_f32 v[82:83], v[170:171], v[94:95] op_sel_hi:[1,0]
	v_pk_mul_f32 v[84:85], v[160:161], v[94:95] op_sel_hi:[1,0]
	v_pk_mul_f32 v[86:87], v[162:163], v[94:95] op_sel_hi:[1,0]
	v_exp_f32_e32 v80, v80
	v_exp_f32_e32 v81, v81
	v_exp_f32_e32 v82, v82
	v_exp_f32_e32 v83, v83
	v_exp_f32_e32 v84, v84
	v_exp_f32_e32 v85, v85
	v_exp_f32_e32 v86, v86
	v_exp_f32_e32 v87, v87
	v_pk_mul_f32 v[168:169], v[172:173], v[168:169]
	v_pk_mul_f32 v[170:171], v[174:175], v[170:171]
	v_pk_mul_f32 v[160:161], v[164:165], v[160:161]
	v_pk_mul_f32 v[162:163], v[166:167], v[162:163]
	v_pk_fma_f32 v[80:81], v[80:81], v[24:25], v[24:25] op_sel_hi:[1,0,0]
	v_pk_fma_f32 v[82:83], v[82:83], v[24:25], v[24:25] op_sel_hi:[1,0,0]
	v_pk_fma_f32 v[84:85], v[84:85], v[24:25], v[24:25] op_sel_hi:[1,0,0]
	v_pk_fma_f32 v[86:87], v[86:87], v[24:25], v[24:25] op_sel_hi:[1,0,0]
	v_rcp_f32_e32 v80, v80
	v_rcp_f32_e32 v81, v81
	v_rcp_f32_e32 v82, v82
	v_rcp_f32_e32 v83, v83
	v_rcp_f32_e32 v84, v84
	v_rcp_f32_e32 v85, v85
	v_rcp_f32_e32 v86, v86
	v_rcp_f32_e32 v87, v87
	v_add_u32_e32 v92, 0x2c000, v232
	v_pk_mul_f32 v[168:169], v[168:169], v[80:81]
	v_pk_mul_f32 v[170:171], v[170:171], v[82:83]
	v_pk_mul_f32 v[160:161], v[160:161], v[84:85]
	v_pk_mul_f32 v[162:163], v[162:163], v[86:87]
	v_cvt_pk_bf16_f32 v88, v168, v169
	v_cvt_pk_bf16_f32 v89, v170, v171
	v_cvt_pk_bf16_f32 v90, v160, v161
	v_cvt_pk_bf16_f32 v91, v162, v163
	global_store_dwordx4 v92, v[88:91], s[8:9]
	v_mul_f32_e32 v78, 0xbfb8aa3b, v226
	v_mul_f32_e32 v20, v226, v226
	v_rcp_f32_e32 v20, v20
	v_cvt_f32_i32_e32 v152, v152
	v_cvt_f32_i32_e32 v153, v153
	v_cvt_f32_i32_e32 v154, v154
	v_cvt_f32_i32_e32 v155, v155
	v_cvt_f32_i32_e32 v144, v144
	v_cvt_f32_i32_e32 v145, v145
	v_cvt_f32_i32_e32 v146, v146
	v_cvt_f32_i32_e32 v147, v147
	v_cvt_f32_i32_e32 v156, v156
	v_cvt_f32_i32_e32 v157, v157
	v_cvt_f32_i32_e32 v158, v158
	v_cvt_f32_i32_e32 v159, v159
	v_cvt_f32_i32_e32 v148, v148
	v_cvt_f32_i32_e32 v149, v149
	v_cvt_f32_i32_e32 v150, v150
	v_cvt_f32_i32_e32 v151, v151
	v_pk_mul_f32 v[64:65], v[152:153], v[78:79] op_sel_hi:[1,0]
	v_pk_mul_f32 v[66:67], v[154:155], v[78:79] op_sel_hi:[1,0]
	v_pk_mul_f32 v[68:69], v[144:145], v[78:79] op_sel_hi:[1,0]
	v_pk_mul_f32 v[70:71], v[146:147], v[78:79] op_sel_hi:[1,0]
	v_exp_f32_e32 v64, v64
	v_exp_f32_e32 v65, v65
	v_exp_f32_e32 v66, v66
	v_exp_f32_e32 v67, v67
	v_exp_f32_e32 v68, v68
	v_exp_f32_e32 v69, v69
	v_exp_f32_e32 v70, v70
	v_exp_f32_e32 v71, v71
	v_pk_mul_f32 v[152:153], v[156:157], v[152:153]
	v_pk_mul_f32 v[154:155], v[158:159], v[154:155]
	v_pk_mul_f32 v[144:145], v[148:149], v[144:145]
	v_pk_mul_f32 v[146:147], v[150:151], v[146:147]
	v_pk_fma_f32 v[64:65], v[64:65], v[20:21], v[20:21] op_sel_hi:[1,0,0]
	v_pk_fma_f32 v[66:67], v[66:67], v[20:21], v[20:21] op_sel_hi:[1,0,0]
	v_pk_fma_f32 v[68:69], v[68:69], v[20:21], v[20:21] op_sel_hi:[1,0,0]
	v_pk_fma_f32 v[70:71], v[70:71], v[20:21], v[20:21] op_sel_hi:[1,0,0]
	v_rcp_f32_e32 v64, v64
	v_rcp_f32_e32 v65, v65
	v_rcp_f32_e32 v66, v66
	v_rcp_f32_e32 v67, v67
	v_rcp_f32_e32 v68, v68
	v_rcp_f32_e32 v69, v69
	v_rcp_f32_e32 v70, v70
	v_rcp_f32_e32 v71, v71
	v_add_u32_e32 v76, 0x58000, v232
	v_pk_mul_f32 v[152:153], v[152:153], v[64:65]
	v_pk_mul_f32 v[154:155], v[154:155], v[66:67]
	v_pk_mul_f32 v[144:145], v[144:145], v[68:69]
	v_pk_mul_f32 v[146:147], v[146:147], v[70:71]
	v_cvt_pk_bf16_f32 v72, v152, v153
	v_cvt_pk_bf16_f32 v73, v154, v155
	v_cvt_pk_bf16_f32 v74, v144, v145
	v_cvt_pk_bf16_f32 v75, v146, v147
	global_store_dwordx4 v76, v[72:75], s[8:9]
	v_mul_f32_e32 v94, 0xbfb8aa3b, v227
	v_mul_f32_e32 v24, v227, v227
	v_rcp_f32_e32 v24, v24
	v_cvt_f32_i32_e32 v136, v136
	v_cvt_f32_i32_e32 v137, v137
	v_cvt_f32_i32_e32 v138, v138
	v_cvt_f32_i32_e32 v139, v139
	v_cvt_f32_i32_e32 v128, v128
	v_cvt_f32_i32_e32 v129, v129
	v_cvt_f32_i32_e32 v130, v130
	v_cvt_f32_i32_e32 v131, v131
	v_cvt_f32_i32_e32 v140, v140
	v_cvt_f32_i32_e32 v141, v141
	v_cvt_f32_i32_e32 v142, v142
	v_cvt_f32_i32_e32 v143, v143
	v_cvt_f32_i32_e32 v132, v132
	v_cvt_f32_i32_e32 v133, v133
	v_cvt_f32_i32_e32 v134, v134
	v_cvt_f32_i32_e32 v135, v135
	v_pk_mul_f32 v[80:81], v[136:137], v[94:95] op_sel_hi:[1,0]
	v_pk_mul_f32 v[82:83], v[138:139], v[94:95] op_sel_hi:[1,0]
	v_pk_mul_f32 v[84:85], v[128:129], v[94:95] op_sel_hi:[1,0]
	v_pk_mul_f32 v[86:87], v[130:131], v[94:95] op_sel_hi:[1,0]
	v_exp_f32_e32 v80, v80
	v_exp_f32_e32 v81, v81
	v_exp_f32_e32 v82, v82
	v_exp_f32_e32 v83, v83
	v_exp_f32_e32 v84, v84
	v_exp_f32_e32 v85, v85
	v_exp_f32_e32 v86, v86
	v_exp_f32_e32 v87, v87
	v_pk_mul_f32 v[136:137], v[140:141], v[136:137]
	v_pk_mul_f32 v[138:139], v[142:143], v[138:139]
	v_pk_mul_f32 v[128:129], v[132:133], v[128:129]
	v_pk_mul_f32 v[130:131], v[134:135], v[130:131]
	v_pk_fma_f32 v[80:81], v[80:81], v[24:25], v[24:25] op_sel_hi:[1,0,0]
	v_pk_fma_f32 v[82:83], v[82:83], v[24:25], v[24:25] op_sel_hi:[1,0,0]
	v_pk_fma_f32 v[84:85], v[84:85], v[24:25], v[24:25] op_sel_hi:[1,0,0]
	v_pk_fma_f32 v[86:87], v[86:87], v[24:25], v[24:25] op_sel_hi:[1,0,0]
	v_rcp_f32_e32 v80, v80
	v_rcp_f32_e32 v81, v81
	v_rcp_f32_e32 v82, v82
	v_rcp_f32_e32 v83, v83
	v_rcp_f32_e32 v84, v84
	v_rcp_f32_e32 v85, v85
	v_rcp_f32_e32 v86, v86
	v_rcp_f32_e32 v87, v87
	v_add_u32_e32 v92, 0x84000, v232
	v_pk_mul_f32 v[136:137], v[136:137], v[80:81]
	v_pk_mul_f32 v[138:139], v[138:139], v[82:83]
	v_pk_mul_f32 v[128:129], v[128:129], v[84:85]
	v_pk_mul_f32 v[130:131], v[130:131], v[86:87]
	v_cvt_pk_bf16_f32 v88, v136, v137
	v_cvt_pk_bf16_f32 v89, v138, v139
	v_cvt_pk_bf16_f32 v90, v128, v129
	v_cvt_pk_bf16_f32 v91, v130, v131
	global_store_dwordx4 v92, v[88:91], s[8:9]
	v_mul_f32_e32 v78, 0xbfb8aa3b, v228
	v_mul_f32_e32 v20, v228, v228
	v_rcp_f32_e32 v20, v20
	v_cvt_f32_i32_e32 v120, v120
	v_cvt_f32_i32_e32 v121, v121
	v_cvt_f32_i32_e32 v122, v122
	v_cvt_f32_i32_e32 v123, v123
	v_cvt_f32_i32_e32 v112, v112
	v_cvt_f32_i32_e32 v113, v113
	v_cvt_f32_i32_e32 v114, v114
	v_cvt_f32_i32_e32 v115, v115
	v_cvt_f32_i32_e32 v124, v124
	v_cvt_f32_i32_e32 v125, v125
	v_cvt_f32_i32_e32 v126, v126
	v_cvt_f32_i32_e32 v127, v127
	v_cvt_f32_i32_e32 v116, v116
	v_cvt_f32_i32_e32 v117, v117
	v_cvt_f32_i32_e32 v118, v118
	v_cvt_f32_i32_e32 v119, v119
	v_pk_mul_f32 v[64:65], v[120:121], v[78:79] op_sel_hi:[1,0]
	v_pk_mul_f32 v[66:67], v[122:123], v[78:79] op_sel_hi:[1,0]
	v_pk_mul_f32 v[68:69], v[112:113], v[78:79] op_sel_hi:[1,0]
	v_pk_mul_f32 v[70:71], v[114:115], v[78:79] op_sel_hi:[1,0]
	v_exp_f32_e32 v64, v64
	v_exp_f32_e32 v65, v65
	v_exp_f32_e32 v66, v66
	v_exp_f32_e32 v67, v67
	v_exp_f32_e32 v68, v68
	v_exp_f32_e32 v69, v69
	v_exp_f32_e32 v70, v70
	v_exp_f32_e32 v71, v71
	v_pk_mul_f32 v[120:121], v[124:125], v[120:121]
	v_pk_mul_f32 v[122:123], v[126:127], v[122:123]
	v_pk_mul_f32 v[112:113], v[116:117], v[112:113]
	v_pk_mul_f32 v[114:115], v[118:119], v[114:115]
	v_pk_fma_f32 v[64:65], v[64:65], v[20:21], v[20:21] op_sel_hi:[1,0,0]
	v_pk_fma_f32 v[66:67], v[66:67], v[20:21], v[20:21] op_sel_hi:[1,0,0]
	v_pk_fma_f32 v[68:69], v[68:69], v[20:21], v[20:21] op_sel_hi:[1,0,0]
	v_pk_fma_f32 v[70:71], v[70:71], v[20:21], v[20:21] op_sel_hi:[1,0,0]
	v_rcp_f32_e32 v64, v64
	v_rcp_f32_e32 v65, v65
	v_rcp_f32_e32 v66, v66
	v_rcp_f32_e32 v67, v67
	v_rcp_f32_e32 v68, v68
	v_rcp_f32_e32 v69, v69
	v_rcp_f32_e32 v70, v70
	v_rcp_f32_e32 v71, v71
	v_add_u32_e32 v76, 0x160000, v232
	v_pk_mul_f32 v[120:121], v[120:121], v[64:65]
	v_pk_mul_f32 v[122:123], v[122:123], v[66:67]
	v_pk_mul_f32 v[112:113], v[112:113], v[68:69]
	v_pk_mul_f32 v[114:115], v[114:115], v[70:71]
	v_cvt_pk_bf16_f32 v72, v120, v121
	v_cvt_pk_bf16_f32 v73, v122, v123
	v_cvt_pk_bf16_f32 v74, v112, v113
	v_cvt_pk_bf16_f32 v75, v114, v115
	global_store_dwordx4 v76, v[72:75], s[8:9]
	v_mul_f32_e32 v94, 0xbfb8aa3b, v229
	v_mul_f32_e32 v24, v229, v229
	v_rcp_f32_e32 v24, v24
	v_cvt_f32_i32_e32 v104, v104
	v_cvt_f32_i32_e32 v105, v105
	v_cvt_f32_i32_e32 v106, v106
	v_cvt_f32_i32_e32 v107, v107
	v_cvt_f32_i32_e32 v96, v96
	v_cvt_f32_i32_e32 v97, v97
	v_cvt_f32_i32_e32 v98, v98
	v_cvt_f32_i32_e32 v99, v99
	v_cvt_f32_i32_e32 v108, v108
	v_cvt_f32_i32_e32 v109, v109
	v_cvt_f32_i32_e32 v110, v110
	v_cvt_f32_i32_e32 v111, v111
	v_cvt_f32_i32_e32 v100, v100
	v_cvt_f32_i32_e32 v101, v101
	v_cvt_f32_i32_e32 v102, v102
	v_cvt_f32_i32_e32 v103, v103
	v_pk_mul_f32 v[80:81], v[104:105], v[94:95] op_sel_hi:[1,0]
	v_pk_mul_f32 v[82:83], v[106:107], v[94:95] op_sel_hi:[1,0]
	v_pk_mul_f32 v[84:85], v[96:97], v[94:95] op_sel_hi:[1,0]
	v_pk_mul_f32 v[86:87], v[98:99], v[94:95] op_sel_hi:[1,0]
	v_exp_f32_e32 v80, v80
	v_exp_f32_e32 v81, v81
	v_exp_f32_e32 v82, v82
	v_exp_f32_e32 v83, v83
	v_exp_f32_e32 v84, v84
	v_exp_f32_e32 v85, v85
	v_exp_f32_e32 v86, v86
	v_exp_f32_e32 v87, v87
	v_pk_mul_f32 v[104:105], v[108:109], v[104:105]
	v_pk_mul_f32 v[106:107], v[110:111], v[106:107]
	v_pk_mul_f32 v[96:97], v[100:101], v[96:97]
	v_pk_mul_f32 v[98:99], v[102:103], v[98:99]
	v_pk_fma_f32 v[80:81], v[80:81], v[24:25], v[24:25] op_sel_hi:[1,0,0]
	v_pk_fma_f32 v[82:83], v[82:83], v[24:25], v[24:25] op_sel_hi:[1,0,0]
	v_pk_fma_f32 v[84:85], v[84:85], v[24:25], v[24:25] op_sel_hi:[1,0,0]
	v_pk_fma_f32 v[86:87], v[86:87], v[24:25], v[24:25] op_sel_hi:[1,0,0]
	v_rcp_f32_e32 v80, v80
	v_rcp_f32_e32 v81, v81
	v_rcp_f32_e32 v82, v82
	v_rcp_f32_e32 v83, v83
	v_rcp_f32_e32 v84, v84
	v_rcp_f32_e32 v85, v85
	v_rcp_f32_e32 v86, v86
	v_rcp_f32_e32 v87, v87
	v_add_u32_e32 v92, 0x18c000, v232
	v_pk_mul_f32 v[104:105], v[104:105], v[80:81]
	v_pk_mul_f32 v[106:107], v[106:107], v[82:83]
	v_pk_mul_f32 v[96:97], v[96:97], v[84:85]
	v_pk_mul_f32 v[98:99], v[98:99], v[86:87]
	v_cvt_pk_bf16_f32 v88, v104, v105
	v_cvt_pk_bf16_f32 v89, v106, v107
	v_cvt_pk_bf16_f32 v90, v96, v97
	v_cvt_pk_bf16_f32 v91, v98, v99
	global_store_dwordx4 v92, v[88:91], s[8:9]
	v_mul_f32_e32 v78, 0xbfb8aa3b, v230
	v_mul_f32_e32 v20, v230, v230
	v_rcp_f32_e32 v20, v20
	v_cvt_f32_i32_e32 v48, v48
	v_cvt_f32_i32_e32 v49, v49
	v_cvt_f32_i32_e32 v50, v50
	v_cvt_f32_i32_e32 v51, v51
	v_cvt_f32_i32_e32 v16, v16
	v_cvt_f32_i32_e32 v17, v17
	v_cvt_f32_i32_e32 v18, v18
	v_cvt_f32_i32_e32 v19, v19
	v_cvt_f32_i32_e32 v60, v60
	v_cvt_f32_i32_e32 v61, v61
	v_cvt_f32_i32_e32 v62, v62
	v_cvt_f32_i32_e32 v63, v63
	v_cvt_f32_i32_e32 v44, v44
	v_cvt_f32_i32_e32 v45, v45
	v_cvt_f32_i32_e32 v46, v46
	v_cvt_f32_i32_e32 v47, v47
	v_pk_mul_f32 v[64:65], v[48:49], v[78:79] op_sel_hi:[1,0]
	v_pk_mul_f32 v[66:67], v[50:51], v[78:79] op_sel_hi:[1,0]
	v_pk_mul_f32 v[68:69], v[16:17], v[78:79] op_sel_hi:[1,0]
	v_pk_mul_f32 v[70:71], v[18:19], v[78:79] op_sel_hi:[1,0]
	v_exp_f32_e32 v64, v64
	v_exp_f32_e32 v65, v65
	v_exp_f32_e32 v66, v66
	v_exp_f32_e32 v67, v67
	v_exp_f32_e32 v68, v68
	v_exp_f32_e32 v69, v69
	v_exp_f32_e32 v70, v70
	v_exp_f32_e32 v71, v71
	v_pk_mul_f32 v[48:49], v[60:61], v[48:49]
	v_pk_mul_f32 v[50:51], v[62:63], v[50:51]
	v_pk_mul_f32 v[16:17], v[44:45], v[16:17]
	v_pk_mul_f32 v[18:19], v[46:47], v[18:19]
	v_pk_fma_f32 v[64:65], v[64:65], v[20:21], v[20:21] op_sel_hi:[1,0,0]
	v_pk_fma_f32 v[66:67], v[66:67], v[20:21], v[20:21] op_sel_hi:[1,0,0]
	v_pk_fma_f32 v[68:69], v[68:69], v[20:21], v[20:21] op_sel_hi:[1,0,0]
	v_pk_fma_f32 v[70:71], v[70:71], v[20:21], v[20:21] op_sel_hi:[1,0,0]
	v_rcp_f32_e32 v64, v64
	v_rcp_f32_e32 v65, v65
	v_rcp_f32_e32 v66, v66
	v_rcp_f32_e32 v67, v67
	v_rcp_f32_e32 v68, v68
	v_rcp_f32_e32 v69, v69
	v_rcp_f32_e32 v70, v70
	v_rcp_f32_e32 v71, v71
	v_add_u32_e32 v76, 0x1b8000, v232
	v_pk_mul_f32 v[48:49], v[48:49], v[64:65]
	v_pk_mul_f32 v[50:51], v[50:51], v[66:67]
	v_pk_mul_f32 v[16:17], v[16:17], v[68:69]
	v_pk_mul_f32 v[18:19], v[18:19], v[70:71]
	v_cvt_pk_bf16_f32 v72, v48, v49
	v_cvt_pk_bf16_f32 v73, v50, v51
	v_cvt_pk_bf16_f32 v74, v16, v17
	v_cvt_pk_bf16_f32 v75, v18, v19
	global_store_dwordx4 v76, v[72:75], s[8:9]
	v_mul_f32_e32 v94, 0xbfb8aa3b, v231
	v_mul_f32_e32 v24, v231, v231
	v_rcp_f32_e32 v24, v24
	v_cvt_f32_i32_e32 v8, v8
	v_cvt_f32_i32_e32 v9, v9
	v_cvt_f32_i32_e32 v10, v10
	v_cvt_f32_i32_e32 v11, v11
	v_cvt_f32_i32_e32 v0, v0
	v_cvt_f32_i32_e32 v1, v1
	v_cvt_f32_i32_e32 v2, v2
	v_cvt_f32_i32_e32 v3, v3
	v_cvt_f32_i32_e32 v12, v12
	v_cvt_f32_i32_e32 v13, v13
	v_cvt_f32_i32_e32 v14, v14
	v_cvt_f32_i32_e32 v15, v15
	v_cvt_f32_i32_e32 v4, v4
	v_cvt_f32_i32_e32 v5, v5
	v_cvt_f32_i32_e32 v6, v6
	v_cvt_f32_i32_e32 v7, v7
	v_pk_mul_f32 v[80:81], v[8:9], v[94:95] op_sel_hi:[1,0]
	v_pk_mul_f32 v[82:83], v[10:11], v[94:95] op_sel_hi:[1,0]
	v_pk_mul_f32 v[84:85], v[0:1], v[94:95] op_sel_hi:[1,0]
	v_pk_mul_f32 v[86:87], v[2:3], v[94:95] op_sel_hi:[1,0]
	v_exp_f32_e32 v80, v80
	v_exp_f32_e32 v81, v81
	v_exp_f32_e32 v82, v82
	v_exp_f32_e32 v83, v83
	v_exp_f32_e32 v84, v84
	v_exp_f32_e32 v85, v85
	v_exp_f32_e32 v86, v86
	v_exp_f32_e32 v87, v87
	v_pk_mul_f32 v[8:9], v[12:13], v[8:9]
	v_pk_mul_f32 v[10:11], v[14:15], v[10:11]
	v_pk_mul_f32 v[0:1], v[4:5], v[0:1]
	v_pk_mul_f32 v[2:3], v[6:7], v[2:3]
	v_pk_fma_f32 v[80:81], v[80:81], v[24:25], v[24:25] op_sel_hi:[1,0,0]
	v_pk_fma_f32 v[82:83], v[82:83], v[24:25], v[24:25] op_sel_hi:[1,0,0]
	v_pk_fma_f32 v[84:85], v[84:85], v[24:25], v[24:25] op_sel_hi:[1,0,0]
	v_pk_fma_f32 v[86:87], v[86:87], v[24:25], v[24:25] op_sel_hi:[1,0,0]
	v_rcp_f32_e32 v80, v80
	v_rcp_f32_e32 v81, v81
	v_rcp_f32_e32 v82, v82
	v_rcp_f32_e32 v83, v83
	v_rcp_f32_e32 v84, v84
	v_rcp_f32_e32 v85, v85
	v_rcp_f32_e32 v86, v86
	v_rcp_f32_e32 v87, v87
	v_add_u32_e32 v92, 0x1e4000, v232
	v_pk_mul_f32 v[8:9], v[8:9], v[80:81]
	v_pk_mul_f32 v[10:11], v[10:11], v[82:83]
	v_pk_mul_f32 v[0:1], v[0:1], v[84:85]
	v_pk_mul_f32 v[2:3], v[2:3], v[86:87]
	v_cvt_pk_bf16_f32 v88, v8, v9
	v_cvt_pk_bf16_f32 v89, v10, v11
	v_cvt_pk_bf16_f32 v90, v0, v1
	v_cvt_pk_bf16_f32 v91, v2, v3
	global_store_dwordx4 v92, v[88:91], s[8:9]
	s_andn2_b64 vcc, exec, s[4:5]
	s_mov_b64 s[4:5], -1
	s_cbranch_vccnz .LBB0_749
	s_andn2_b64 vcc, exec, s[6:7]
	s_cbranch_vccnz .LBB0_748
	s_branch .LBB0_748

.LBB0_1411:
	ds_read_b128 v[146:149], v138
	ds_read_b128 v[150:153], v138 offset:1024
	ds_read_b128 v[154:157], v138 offset:2048
	ds_read_b128 v[158:161], v138 offset:3072
	ds_read_b128 v[162:165], v139
	ds_read_b128 v[166:169], v139 offset:1024
	ds_read_b128 v[170:173], v139 offset:2048
	ds_read_b128 v[174:177], v139 offset:3072
	ds_read_b128 v[178:181], v140
	ds_read_b128 v[182:185], v140 offset:1024
	ds_read_b128 v[186:189], v140 offset:2048
	ds_read_b128 v[190:193], v140 offset:3072
	ds_read_b128 v[194:197], v140 offset:4096
	ds_read_b128 v[198:201], v140 offset:5120
	ds_read_b128 v[202:205], v140 offset:6144
	ds_read_b128 v[206:209], v140 offset:7168
	s_add_u32 s26, s6, 0x100
	s_addc_u32 s27, s7, 0
	s_cmp_eq_u32 s55, 12
	s_cselect_b32 s36, s15, s26
	s_cselect_b32 s37, s2, s27
	s_cselect_b32 s30, s18, s17
	s_cselect_b32 s31, s19, s54
	s_add_u32 s28, s36, 0x80
	s_addc_u32 s29, s37, 0
	s_add_u32 s34, s30, 0x80
	s_addc_u32 s35, s31, 0
	s_add_u32 s6, s6, 0x40080
	s_addc_u32 s7, s7, 0
	s_add_i32 m0, s47, 0xc000
	s_nop 0
	global_load_lds_dwordx4 v134, s[6:7]
	s_nop 0
	s_add_i32 m0, s47, 0xe000
	s_nop 0
	global_load_lds_dwordx4 v136, s[6:7]
	s_waitcnt vmcnt(8)
	s_waitcnt lgkmcnt(0)
	s_barrier
	v_mfma_f32_16x16x128_f8f6f4 v[112:115], v[146:153], v[178:185], v[112:115]
	v_mfma_f32_16x16x128_f8f6f4 v[116:119], v[154:161], v[178:185], v[116:119]
	v_mfma_f32_16x16x128_f8f6f4 v[96:99], v[154:161], v[186:193], v[96:99]
	v_mfma_f32_16x16x128_f8f6f4 v[100:103], v[146:153], v[186:193], v[100:103]
	v_mfma_f32_16x16x128_f8f6f4 v[210:213], v[146:153], v[194:201], v[84:87]
	v_mfma_f32_16x16x128_f8f6f4 v[214:217], v[154:161], v[194:201], v[80:83]
	v_mfma_f32_16x16x128_f8f6f4 v[222:225], v[154:161], v[202:209], v[56:59]
	v_mfma_f32_16x16x128_f8f6f4 v[218:221], v[146:153], v[202:209], v[60:63]
	v_mfma_f32_16x16x128_f8f6f4 v[120:123], v[162:169], v[178:185], v[120:123]
	v_mfma_f32_16x16x128_f8f6f4 v[124:127], v[170:177], v[178:185], v[124:127]
	v_mfma_f32_16x16x128_f8f6f4 v[108:111], v[162:169], v[186:193], v[108:111]
	v_mfma_f32_16x16x128_f8f6f4 v[104:107], v[170:177], v[186:193], v[104:107]
	v_mfma_f32_16x16x128_f8f6f4 v[178:181], v[162:169], v[194:201], v[92:95]
	v_mfma_f32_16x16x128_f8f6f4 v[182:185], v[170:177], v[194:201], v[88:91]
	v_mfma_f32_16x16x128_f8f6f4 v[186:189], v[162:169], v[202:209], v[76:79]
	v_mfma_f32_16x16x128_f8f6f4 v[190:193], v[170:177], v[202:209], v[72:75]
	s_barrier
	ds_read_b128 v[56:59], v140 offset:16384
	ds_read_b128 v[60:63], v140 offset:17408
	s_nop 2
	ds_read_b128 v[72:75], v140 offset:18432
	ds_read_b128 v[76:79], v140 offset:19456
	ds_read_b128 v[80:83], v140 offset:20480
	ds_read_b128 v[84:87], v140 offset:21504
	ds_read_b128 v[88:91], v140 offset:22528
	ds_read_b128 v[92:95], v140 offset:23552
	s_add_i32 m0, s47, 0x10000
	s_nop 0
	global_load_lds_dwordx4 v135, s[30:31]
	s_nop 0
	s_add_i32 m0, s47, 0x12000
	s_nop 0
	global_load_lds_dwordx4 v137, s[30:31]
	s_add_u32 s6, s30, 0x40000
	s_addc_u32 s7, s31, 0
	s_add_i32 m0, s47, 0x14000
	s_nop 0
	global_load_lds_dwordx4 v135, s[6:7]
	s_nop 0
	s_add_i32 m0, s47, 0x16000
	s_nop 0
	global_load_lds_dwordx4 v137, s[6:7]
	s_nop 0
	s_add_i32 m0, s47, 0
	s_nop 0
	global_load_lds_dwordx4 v134, s[36:37]
	s_nop 0
	s_add_i32 m0, s47, 0x2000
	s_nop 0
	global_load_lds_dwordx4 v136, s[36:37]
	s_waitcnt vmcnt(8)
	s_waitcnt lgkmcnt(0)
	s_barrier
	v_mfma_f32_16x16x128_f8f6f4 v[52:55], v[146:153], v[56:63], v[52:55]
	v_mfma_f32_16x16x128_f8f6f4 v[48:51], v[154:161], v[56:63], v[48:51]
	v_mfma_f32_16x16x128_f8f6f4 v[198:201], v[154:161], v[72:79], v[32:35]
	v_mfma_f32_16x16x128_f8f6f4 v[194:197], v[146:153], v[72:79], v[36:39]
	v_mfma_f32_16x16x128_f8f6f4 v[202:205], v[146:153], v[80:87], v[20:23]
	v_mfma_f32_16x16x128_f8f6f4 v[206:209], v[154:161], v[80:87], v[16:19]
	v_mfma_f32_16x16x128_f8f6f4 v[230:233], v[154:161], v[88:95], v[0:3]
	v_mfma_f32_16x16x128_f8f6f4 v[226:229], v[146:153], v[88:95], v[4:7]
	v_mfma_f32_16x16x128_f8f6f4 v[68:71], v[162:169], v[56:63], v[68:71]
	v_mfma_f32_16x16x128_f8f6f4 v[64:67], v[170:177], v[56:63], v[64:67]
	v_mfma_f32_16x16x128_f8f6f4 v[238:241], v[170:177], v[72:79], v[40:43]
	v_mfma_f32_16x16x128_f8f6f4 v[234:237], v[162:169], v[72:79], v[44:47]
	v_mfma_f32_16x16x128_f8f6f4 v[242:245], v[162:169], v[80:87], v[28:31]
	v_mfma_f32_16x16x128_f8f6f4 v[246:249], v[170:177], v[80:87], v[24:27]
	v_mfma_f32_16x16x128_f8f6f4 v[130:133], v[170:177], v[88:95], v[8:11]
	v_mfma_f32_16x16x128_f8f6f4 v[250:253], v[162:169], v[88:95], v[12:15]
	s_barrier
	ds_read_b128 v[0:3], v141
	ds_read_b128 v[4:7], v141 offset:1024
	s_nop 2
	ds_read_b128 v[8:11], v141 offset:2048
	ds_read_b128 v[12:15], v141 offset:3072
	ds_read_b128 v[146:149], v142
	ds_read_b128 v[150:153], v142 offset:1024
	ds_read_b128 v[154:157], v142 offset:2048
	ds_read_b128 v[158:161], v142 offset:3072
	ds_read_b128 v[16:19], v140 offset:32768
	ds_read_b128 v[20:23], v140 offset:33792
	ds_read_b128 v[24:27], v140 offset:34816
	ds_read_b128 v[28:31], v140 offset:35840
	ds_read_b128 v[32:35], v140 offset:36864
	ds_read_b128 v[36:39], v140 offset:37888
	ds_read_b128 v[40:43], v140 offset:38912
	ds_read_b128 v[44:47], v140 offset:39936
	s_add_u32 s6, s36, 0x40000
	s_addc_u32 s7, s37, 0
	s_add_i32 m0, s47, 0x4000
	s_nop 0
	global_load_lds_dwordx4 v134, s[6:7]
	s_nop 0
	s_add_i32 m0, s47, 0x6000
	s_nop 0
	global_load_lds_dwordx4 v136, s[6:7]
	s_waitcnt vmcnt(8)
	s_waitcnt lgkmcnt(0)
	s_barrier
	v_mfma_f32_16x16x128_f8f6f4 v[112:115], v[0:7], v[16:23], v[112:115]
	v_mfma_f32_16x16x128_f8f6f4 v[116:119], v[8:15], v[16:23], v[116:119]
	v_mfma_f32_16x16x128_f8f6f4 v[96:99], v[8:15], v[24:31], v[96:99]
	v_mfma_f32_16x16x128_f8f6f4 v[100:103], v[0:7], v[24:31], v[100:103]
	v_mfma_f32_16x16x128_f8f6f4 v[84:87], v[0:7], v[32:39], v[210:213]
	v_mfma_f32_16x16x128_f8f6f4 v[80:83], v[8:15], v[32:39], v[214:217]
	v_mfma_f32_16x16x128_f8f6f4 v[56:59], v[8:15], v[40:47], v[222:225]
	v_mfma_f32_16x16x128_f8f6f4 v[60:63], v[0:7], v[40:47], v[218:221]
	v_mfma_f32_16x16x128_f8f6f4 v[120:123], v[146:153], v[16:23], v[120:123]
	v_mfma_f32_16x16x128_f8f6f4 v[124:127], v[154:161], v[16:23], v[124:127]
	v_mfma_f32_16x16x128_f8f6f4 v[104:107], v[154:161], v[24:31], v[104:107]
	v_mfma_f32_16x16x128_f8f6f4 v[108:111], v[146:153], v[24:31], v[108:111]
	v_mfma_f32_16x16x128_f8f6f4 v[92:95], v[146:153], v[32:39], v[178:181]
	v_mfma_f32_16x16x128_f8f6f4 v[88:91], v[154:161], v[32:39], v[182:185]
	v_mfma_f32_16x16x128_f8f6f4 v[72:75], v[154:161], v[40:47], v[190:193]
	v_mfma_f32_16x16x128_f8f6f4 v[76:79], v[146:153], v[40:47], v[186:189]
	s_barrier
	ds_read_b128 v[24:27], v140 offset:49152
	ds_read_b128 v[28:31], v140 offset:50176
	ds_read_b128 v[162:165], v140 offset:51200
	ds_read_b128 v[166:169], v140 offset:52224
	ds_read_b128 v[170:173], v140 offset:53248
	ds_read_b128 v[174:177], v140 offset:54272
	ds_read_b128 v[178:181], v140 offset:55296
	ds_read_b128 v[182:185], v140 offset:56320
	s_add_i32 m0, s47, 0x18000
	s_nop 0
	global_load_lds_dwordx4 v135, s[34:35]
	s_nop 0
	s_add_i32 m0, s47, 0x1a000
	s_nop 0
	global_load_lds_dwordx4 v137, s[34:35]
	s_add_u32 s6, s30, 0x40080
	s_addc_u32 s7, s31, 0
	s_add_i32 m0, s47, 0x1c000
	s_nop 0
	global_load_lds_dwordx4 v135, s[6:7]
	s_nop 0
	s_add_i32 m0, s47, 0x1e000
	s_nop 0
	global_load_lds_dwordx4 v137, s[6:7]
	s_nop 0
	s_add_i32 m0, s47, 0x8000
	s_nop 0
	global_load_lds_dwordx4 v134, s[28:29]
	s_nop 0
	s_add_i32 m0, s47, 0xa000
	s_nop 0
	global_load_lds_dwordx4 v136, s[28:29]
	s_waitcnt vmcnt(8)
	s_waitcnt lgkmcnt(0)
	s_barrier
	v_mfma_f32_16x16x128_f8f6f4 v[52:55], v[0:7], v[24:31], v[52:55]
	v_mfma_f32_16x16x128_f8f6f4 v[48:51], v[8:15], v[24:31], v[48:51]
	v_mfma_f32_16x16x128_f8f6f4 v[36:39], v[0:7], v[162:169], v[194:197]
	v_mfma_f32_16x16x128_f8f6f4 v[32:35], v[8:15], v[162:169], v[198:201]
	v_mfma_f32_16x16x128_f8f6f4 v[20:23], v[0:7], v[170:177], v[202:205]
	v_mfma_f32_16x16x128_f8f6f4 v[16:19], v[8:15], v[170:177], v[206:209]
	v_mfma_f32_16x16x128_f8f6f4 v[4:7], v[0:7], v[178:185], v[226:229]
	v_mfma_f32_16x16x128_f8f6f4 v[0:3], v[8:15], v[178:185], v[230:233]
	v_mfma_f32_16x16x128_f8f6f4 v[68:71], v[146:153], v[24:31], v[68:71]
	v_mfma_f32_16x16x128_f8f6f4 v[64:67], v[154:161], v[24:31], v[64:67]
	v_mfma_f32_16x16x128_f8f6f4 v[44:47], v[146:153], v[162:169], v[234:237]
	v_mfma_f32_16x16x128_f8f6f4 v[40:43], v[154:161], v[162:169], v[238:241]
	v_mfma_f32_16x16x128_f8f6f4 v[28:31], v[146:153], v[170:177], v[242:245]
	v_mfma_f32_16x16x128_f8f6f4 v[24:27], v[154:161], v[170:177], v[246:249]
	v_mfma_f32_16x16x128_f8f6f4 v[12:15], v[146:153], v[178:185], v[250:253]
	v_mfma_f32_16x16x128_f8f6f4 v[8:11], v[154:161], v[178:185], v[130:133]
	s_barrier
	s_add_i32 s55, s55, 2
	s_add_u32 s17, s17, 0x100
	s_addc_u32 s54, s54, 0
	s_cmp_gt_u32 s55, 13
	s_mov_b64 s[6:7], s[26:27]
	s_cbranch_scc0 .LBB0_1411
	s_and_b64 vcc, s[12:13], s[4:5]
	s_cbranch_vccz .LBB0_1414
	s_barrier
.LBB0_1414:
	s_lshl_b32 s2, s24, 8
	s_add_i32 s2, s2, s25
	v_and_or_b32 v145, v254, 15, s2
	s_lshl_b32 s2, s22, 7
	v_ashrrev_i32_e32 v130, 1, v254
	s_or_b32 s2, s2, s49
	v_and_b32_e32 v130, -8, v130
	v_add_u32_e32 v130, s2, v130
	v_mad_u32_u24 v246, v145, s52, v130
	v_mov_b32_e32 v250, 0xb938aa3b
	v_mov_b32_e32 v251, 0xb938aa3b
	v_mov_b32_e32 v252, 0x4b000000
	v_mov_b32_e32 v253, 0x4b000000
	v_pk_mul_f32 v[146:147], v[112:113], v[250:251]
	v_pk_mul_f32 v[148:149], v[114:115], v[250:251]
	v_pk_mul_f32 v[150:151], v[116:117], v[250:251]
	v_pk_mul_f32 v[152:153], v[118:119], v[250:251]
	v_exp_f32_e32 v146, v146
	v_exp_f32_e32 v147, v147
	v_exp_f32_e32 v148, v148
	v_exp_f32_e32 v149, v149
	v_exp_f32_e32 v150, v150
	v_exp_f32_e32 v151, v151
	v_exp_f32_e32 v152, v152
	v_exp_f32_e32 v153, v153
	v_pk_mul_f32 v[112:113], v[112:113], v[120:121]
	v_pk_mul_f32 v[114:115], v[114:115], v[122:123]
	v_pk_mul_f32 v[116:117], v[116:117], v[124:125]
	v_pk_mul_f32 v[118:119], v[118:119], v[126:127]
	v_pk_fma_f32 v[146:147], v[146:147], v[252:253], v[252:253]
	v_pk_fma_f32 v[148:149], v[148:149], v[252:253], v[252:253]
	v_pk_fma_f32 v[150:151], v[150:151], v[252:253], v[252:253]
	v_pk_fma_f32 v[152:153], v[152:153], v[252:253], v[252:253]
	v_rcp_f32_e32 v146, v146
	v_rcp_f32_e32 v147, v147
	v_rcp_f32_e32 v148, v148
	v_rcp_f32_e32 v149, v149
	v_rcp_f32_e32 v150, v150
	v_rcp_f32_e32 v151, v151
	v_rcp_f32_e32 v152, v152
	v_rcp_f32_e32 v153, v153
	v_mov_b32_e32 v156, v246
	v_pk_mul_f32 v[112:113], v[112:113], v[146:147]
	v_pk_mul_f32 v[114:115], v[114:115], v[148:149]
	v_pk_mul_f32 v[116:117], v[116:117], v[150:151]
	v_pk_mul_f32 v[118:119], v[118:119], v[152:153]
	v_med3_f32 v112, v112, s51, v144
	v_med3_f32 v113, v113, s51, v144
	v_med3_f32 v114, v114, s51, v144
	v_med3_f32 v115, v115, s51, v144
	v_med3_f32 v116, v116, s51, v144
	v_med3_f32 v117, v117, s51, v144
	v_med3_f32 v118, v118, s51, v144
	v_med3_f32 v119, v119, s51, v144
	v_cvt_pk_fp8_f32 v154, v112, v113
	v_cvt_pk_fp8_f32 v155, v116, v117
	v_cvt_pk_fp8_f32 v154, v114, v115 op_sel:[0,0,1]
	v_cvt_pk_fp8_f32 v155, v118, v119 op_sel:[0,0,1]
	s_nop 0
	global_store_dwordx2 v156, v[154:155], s[10:11]
	v_pk_mul_f32 v[160:161], v[100:101], v[250:251]
	v_pk_mul_f32 v[162:163], v[102:103], v[250:251]
	v_pk_mul_f32 v[164:165], v[96:97], v[250:251]
	v_pk_mul_f32 v[166:167], v[98:99], v[250:251]
	v_exp_f32_e32 v160, v160
	v_exp_f32_e32 v161, v161
	v_exp_f32_e32 v162, v162
	v_exp_f32_e32 v163, v163
	v_exp_f32_e32 v164, v164
	v_exp_f32_e32 v165, v165
	v_exp_f32_e32 v166, v166
	v_exp_f32_e32 v167, v167
	v_pk_mul_f32 v[100:101], v[100:101], v[108:109]
	v_pk_mul_f32 v[102:103], v[102:103], v[110:111]
	v_pk_mul_f32 v[96:97], v[96:97], v[104:105]
	v_pk_mul_f32 v[98:99], v[98:99], v[106:107]
	v_pk_fma_f32 v[160:161], v[160:161], v[252:253], v[252:253]
	v_pk_fma_f32 v[162:163], v[162:163], v[252:253], v[252:253]
	v_pk_fma_f32 v[164:165], v[164:165], v[252:253], v[252:253]
	v_pk_fma_f32 v[166:167], v[166:167], v[252:253], v[252:253]
	v_rcp_f32_e32 v160, v160
	v_rcp_f32_e32 v161, v161
	v_rcp_f32_e32 v162, v162
	v_rcp_f32_e32 v163, v163
	v_rcp_f32_e32 v164, v164
	v_rcp_f32_e32 v165, v165
	v_rcp_f32_e32 v166, v166
	v_rcp_f32_e32 v167, v167
	v_add_u32_e32 v170, 0x1c000, v246
	v_pk_mul_f32 v[100:101], v[100:101], v[160:161]
	v_pk_mul_f32 v[102:103], v[102:103], v[162:163]
	v_pk_mul_f32 v[96:97], v[96:97], v[164:165]
	v_pk_mul_f32 v[98:99], v[98:99], v[166:167]
	v_med3_f32 v100, v100, s51, v144
	v_med3_f32 v101, v101, s51, v144
	v_med3_f32 v102, v102, s51, v144
	v_med3_f32 v103, v103, s51, v144
	v_med3_f32 v96, v96, s51, v144
	v_med3_f32 v97, v97, s51, v144
	v_med3_f32 v98, v98, s51, v144
	v_med3_f32 v99, v99, s51, v144
	v_cvt_pk_fp8_f32 v168, v100, v101
	v_cvt_pk_fp8_f32 v169, v96, v97
	v_cvt_pk_fp8_f32 v168, v102, v103 op_sel:[0,0,1]
	v_cvt_pk_fp8_f32 v169, v98, v99 op_sel:[0,0,1]
	s_nop 0
	global_store_dwordx2 v170, v[168:169], s[10:11]
	v_pk_mul_f32 v[146:147], v[84:85], v[250:251]
	v_pk_mul_f32 v[148:149], v[86:87], v[250:251]
	v_pk_mul_f32 v[150:151], v[80:81], v[250:251]
	v_pk_mul_f32 v[152:153], v[82:83], v[250:251]
	v_exp_f32_e32 v146, v146
	v_exp_f32_e32 v147, v147
	v_exp_f32_e32 v148, v148
	v_exp_f32_e32 v149, v149
	v_exp_f32_e32 v150, v150
	v_exp_f32_e32 v151, v151
	v_exp_f32_e32 v152, v152
	v_exp_f32_e32 v153, v153
	v_pk_mul_f32 v[84:85], v[84:85], v[92:93]
	v_pk_mul_f32 v[86:87], v[86:87], v[94:95]
	v_pk_mul_f32 v[80:81], v[80:81], v[88:89]
	v_pk_mul_f32 v[82:83], v[82:83], v[90:91]
	v_pk_fma_f32 v[146:147], v[146:147], v[252:253], v[252:253]
	v_pk_fma_f32 v[148:149], v[148:149], v[252:253], v[252:253]
	v_pk_fma_f32 v[150:151], v[150:151], v[252:253], v[252:253]
	v_pk_fma_f32 v[152:153], v[152:153], v[252:253], v[252:253]
	v_rcp_f32_e32 v146, v146
	v_rcp_f32_e32 v147, v147
	v_rcp_f32_e32 v148, v148
	v_rcp_f32_e32 v149, v149
	v_rcp_f32_e32 v150, v150
	v_rcp_f32_e32 v151, v151
	v_rcp_f32_e32 v152, v152
	v_rcp_f32_e32 v153, v153
	v_add_u32_e32 v156, 0x38000, v246
	v_pk_mul_f32 v[84:85], v[84:85], v[146:147]
	v_pk_mul_f32 v[86:87], v[86:87], v[148:149]
	v_pk_mul_f32 v[80:81], v[80:81], v[150:151]
	v_pk_mul_f32 v[82:83], v[82:83], v[152:153]
	v_med3_f32 v84, v84, s51, v144
	v_med3_f32 v85, v85, s51, v144
	v_med3_f32 v86, v86, s51, v144
	v_med3_f32 v87, v87, s51, v144
	v_med3_f32 v80, v80, s51, v144
	v_med3_f32 v81, v81, s51, v144
	v_med3_f32 v82, v82, s51, v144
	v_med3_f32 v83, v83, s51, v144
	v_cvt_pk_fp8_f32 v154, v84, v85
	v_cvt_pk_fp8_f32 v155, v80, v81
	v_cvt_pk_fp8_f32 v154, v86, v87 op_sel:[0,0,1]
	v_cvt_pk_fp8_f32 v155, v82, v83 op_sel:[0,0,1]
	s_nop 0
	global_store_dwordx2 v156, v[154:155], s[10:11]
	v_pk_mul_f32 v[160:161], v[60:61], v[250:251]
	v_pk_mul_f32 v[162:163], v[62:63], v[250:251]
	v_pk_mul_f32 v[164:165], v[56:57], v[250:251]
	v_pk_mul_f32 v[166:167], v[58:59], v[250:251]
	v_exp_f32_e32 v160, v160
	v_exp_f32_e32 v161, v161
	v_exp_f32_e32 v162, v162
	v_exp_f32_e32 v163, v163
	v_exp_f32_e32 v164, v164
	v_exp_f32_e32 v165, v165
	v_exp_f32_e32 v166, v166
	v_exp_f32_e32 v167, v167
	v_pk_mul_f32 v[60:61], v[60:61], v[76:77]
	v_pk_mul_f32 v[62:63], v[62:63], v[78:79]
	v_pk_mul_f32 v[56:57], v[56:57], v[72:73]
	v_pk_mul_f32 v[58:59], v[58:59], v[74:75]
	v_pk_fma_f32 v[160:161], v[160:161], v[252:253], v[252:253]
	v_pk_fma_f32 v[162:163], v[162:163], v[252:253], v[252:253]
	v_pk_fma_f32 v[164:165], v[164:165], v[252:253], v[252:253]
	v_pk_fma_f32 v[166:167], v[166:167], v[252:253], v[252:253]
	v_rcp_f32_e32 v160, v160
	v_rcp_f32_e32 v161, v161
	v_rcp_f32_e32 v162, v162
	v_rcp_f32_e32 v163, v163
	v_rcp_f32_e32 v164, v164
	v_rcp_f32_e32 v165, v165
	v_rcp_f32_e32 v166, v166
	v_rcp_f32_e32 v167, v167
	v_add_u32_e32 v170, 0x54000, v246
	v_pk_mul_f32 v[60:61], v[60:61], v[160:161]
	v_pk_mul_f32 v[62:63], v[62:63], v[162:163]
	v_pk_mul_f32 v[56:57], v[56:57], v[164:165]
	v_pk_mul_f32 v[58:59], v[58:59], v[166:167]
	v_med3_f32 v60, v60, s51, v144
	v_med3_f32 v61, v61, s51, v144
	v_med3_f32 v62, v62, s51, v144
	v_med3_f32 v63, v63, s51, v144
	v_med3_f32 v56, v56, s51, v144
	v_med3_f32 v57, v57, s51, v144
	v_med3_f32 v58, v58, s51, v144
	v_med3_f32 v59, v59, s51, v144
	v_cvt_pk_fp8_f32 v168, v60, v61
	v_cvt_pk_fp8_f32 v169, v56, v57
	v_cvt_pk_fp8_f32 v168, v62, v63 op_sel:[0,0,1]
	v_cvt_pk_fp8_f32 v169, v58, v59 op_sel:[0,0,1]
	s_nop 0
	global_store_dwordx2 v170, v[168:169], s[10:11]
	v_pk_mul_f32 v[146:147], v[52:53], v[250:251]
	v_pk_mul_f32 v[148:149], v[54:55], v[250:251]
	v_pk_mul_f32 v[150:151], v[48:49], v[250:251]
	v_pk_mul_f32 v[152:153], v[50:51], v[250:251]
	v_exp_f32_e32 v146, v146
	v_exp_f32_e32 v147, v147
	v_exp_f32_e32 v148, v148
	v_exp_f32_e32 v149, v149
	v_exp_f32_e32 v150, v150
	v_exp_f32_e32 v151, v151
	v_exp_f32_e32 v152, v152
	v_exp_f32_e32 v153, v153
	v_pk_mul_f32 v[52:53], v[52:53], v[68:69]
	v_pk_mul_f32 v[54:55], v[54:55], v[70:71]
	v_pk_mul_f32 v[48:49], v[48:49], v[64:65]
	v_pk_mul_f32 v[50:51], v[50:51], v[66:67]
	v_pk_fma_f32 v[146:147], v[146:147], v[252:253], v[252:253]
	v_pk_fma_f32 v[148:149], v[148:149], v[252:253], v[252:253]
	v_pk_fma_f32 v[150:151], v[150:151], v[252:253], v[252:253]
	v_pk_fma_f32 v[152:153], v[152:153], v[252:253], v[252:253]
	v_rcp_f32_e32 v146, v146
	v_rcp_f32_e32 v147, v147
	v_rcp_f32_e32 v148, v148
	v_rcp_f32_e32 v149, v149
	v_rcp_f32_e32 v150, v150
	v_rcp_f32_e32 v151, v151
	v_rcp_f32_e32 v152, v152
	v_rcp_f32_e32 v153, v153
	v_add_u32_e32 v156, 0xe0000, v246
	v_pk_mul_f32 v[52:53], v[52:53], v[146:147]
	v_pk_mul_f32 v[54:55], v[54:55], v[148:149]
	v_pk_mul_f32 v[48:49], v[48:49], v[150:151]
	v_pk_mul_f32 v[50:51], v[50:51], v[152:153]
	v_med3_f32 v52, v52, s51, v144
	v_med3_f32 v53, v53, s51, v144
	v_med3_f32 v54, v54, s51, v144
	v_med3_f32 v55, v55, s51, v144
	v_med3_f32 v48, v48, s51, v144
	v_med3_f32 v49, v49, s51, v144
	v_med3_f32 v50, v50, s51, v144
	v_med3_f32 v51, v51, s51, v144
	v_cvt_pk_fp8_f32 v154, v52, v53
	v_cvt_pk_fp8_f32 v155, v48, v49
	v_cvt_pk_fp8_f32 v154, v54, v55 op_sel:[0,0,1]
	v_cvt_pk_fp8_f32 v155, v50, v51 op_sel:[0,0,1]
	s_nop 0
	global_store_dwordx2 v156, v[154:155], s[10:11]
	v_pk_mul_f32 v[160:161], v[36:37], v[250:251]
	v_pk_mul_f32 v[162:163], v[38:39], v[250:251]
	v_pk_mul_f32 v[164:165], v[32:33], v[250:251]
	v_pk_mul_f32 v[166:167], v[34:35], v[250:251]
	v_exp_f32_e32 v160, v160
	v_exp_f32_e32 v161, v161
	v_exp_f32_e32 v162, v162
	v_exp_f32_e32 v163, v163
	v_exp_f32_e32 v164, v164
	v_exp_f32_e32 v165, v165
	v_exp_f32_e32 v166, v166
	v_exp_f32_e32 v167, v167
	v_pk_mul_f32 v[36:37], v[36:37], v[44:45]
	v_pk_mul_f32 v[38:39], v[38:39], v[46:47]
	v_pk_mul_f32 v[32:33], v[32:33], v[40:41]
	v_pk_mul_f32 v[34:35], v[34:35], v[42:43]
	v_pk_fma_f32 v[160:161], v[160:161], v[252:253], v[252:253]
	v_pk_fma_f32 v[162:163], v[162:163], v[252:253], v[252:253]
	v_pk_fma_f32 v[164:165], v[164:165], v[252:253], v[252:253]
	v_pk_fma_f32 v[166:167], v[166:167], v[252:253], v[252:253]
	v_rcp_f32_e32 v160, v160
	v_rcp_f32_e32 v161, v161
	v_rcp_f32_e32 v162, v162
	v_rcp_f32_e32 v163, v163
	v_rcp_f32_e32 v164, v164
	v_rcp_f32_e32 v165, v165
	v_rcp_f32_e32 v166, v166
	v_rcp_f32_e32 v167, v167
	v_add_u32_e32 v170, 0xfc000, v246
	v_pk_mul_f32 v[36:37], v[36:37], v[160:161]
	v_pk_mul_f32 v[38:39], v[38:39], v[162:163]
	v_pk_mul_f32 v[32:33], v[32:33], v[164:165]
	v_pk_mul_f32 v[34:35], v[34:35], v[166:167]
	v_med3_f32 v36, v36, s51, v144
	v_med3_f32 v37, v37, s51, v144
	v_med3_f32 v38, v38, s51, v144
	v_med3_f32 v39, v39, s51, v144
	v_med3_f32 v32, v32, s51, v144
	v_med3_f32 v33, v33, s51, v144
	v_med3_f32 v34, v34, s51, v144
	v_med3_f32 v35, v35, s51, v144
	v_cvt_pk_fp8_f32 v168, v36, v37
	v_cvt_pk_fp8_f32 v169, v32, v33
	v_cvt_pk_fp8_f32 v168, v38, v39 op_sel:[0,0,1]
	v_cvt_pk_fp8_f32 v169, v34, v35 op_sel:[0,0,1]
	s_nop 0
	global_store_dwordx2 v170, v[168:169], s[10:11]
	v_pk_mul_f32 v[146:147], v[20:21], v[250:251]
	v_pk_mul_f32 v[148:149], v[22:23], v[250:251]
	v_pk_mul_f32 v[150:151], v[16:17], v[250:251]
	v_pk_mul_f32 v[152:153], v[18:19], v[250:251]
	v_exp_f32_e32 v146, v146
	v_exp_f32_e32 v147, v147
	v_exp_f32_e32 v148, v148
	v_exp_f32_e32 v149, v149
	v_exp_f32_e32 v150, v150
	v_exp_f32_e32 v151, v151
	v_exp_f32_e32 v152, v152
	v_exp_f32_e32 v153, v153
	v_pk_mul_f32 v[20:21], v[20:21], v[28:29]
	v_pk_mul_f32 v[22:23], v[22:23], v[30:31]
	v_pk_mul_f32 v[16:17], v[16:17], v[24:25]
	v_pk_mul_f32 v[18:19], v[18:19], v[26:27]
	v_pk_fma_f32 v[146:147], v[146:147], v[252:253], v[252:253]
	v_pk_fma_f32 v[148:149], v[148:149], v[252:253], v[252:253]
	v_pk_fma_f32 v[150:151], v[150:151], v[252:253], v[252:253]
	v_pk_fma_f32 v[152:153], v[152:153], v[252:253], v[252:253]
	v_rcp_f32_e32 v146, v146
	v_rcp_f32_e32 v147, v147
	v_rcp_f32_e32 v148, v148
	v_rcp_f32_e32 v149, v149
	v_rcp_f32_e32 v150, v150
	v_rcp_f32_e32 v151, v151
	v_rcp_f32_e32 v152, v152
	v_rcp_f32_e32 v153, v153
	v_add_u32_e32 v156, 0x118000, v246
	v_pk_mul_f32 v[20:21], v[20:21], v[146:147]
	v_pk_mul_f32 v[22:23], v[22:23], v[148:149]
	v_pk_mul_f32 v[16:17], v[16:17], v[150:151]
	v_pk_mul_f32 v[18:19], v[18:19], v[152:153]
	v_med3_f32 v20, v20, s51, v144
	v_med3_f32 v21, v21, s51, v144
	v_med3_f32 v22, v22, s51, v144
	v_med3_f32 v23, v23, s51, v144
	v_med3_f32 v16, v16, s51, v144
	v_med3_f32 v17, v17, s51, v144
	v_med3_f32 v18, v18, s51, v144
	v_med3_f32 v19, v19, s51, v144
	v_cvt_pk_fp8_f32 v154, v20, v21
	v_cvt_pk_fp8_f32 v155, v16, v17
	v_cvt_pk_fp8_f32 v154, v22, v23 op_sel:[0,0,1]
	v_cvt_pk_fp8_f32 v155, v18, v19 op_sel:[0,0,1]
	s_nop 0
	global_store_dwordx2 v156, v[154:155], s[10:11]
	v_pk_mul_f32 v[160:161], v[4:5], v[250:251]
	v_pk_mul_f32 v[162:163], v[6:7], v[250:251]
	v_pk_mul_f32 v[164:165], v[0:1], v[250:251]
	v_pk_mul_f32 v[166:167], v[2:3], v[250:251]
	v_exp_f32_e32 v160, v160
	v_exp_f32_e32 v161, v161
	v_exp_f32_e32 v162, v162
	v_exp_f32_e32 v163, v163
	v_exp_f32_e32 v164, v164
	v_exp_f32_e32 v165, v165
	v_exp_f32_e32 v166, v166
	v_exp_f32_e32 v167, v167
	v_pk_mul_f32 v[4:5], v[4:5], v[12:13]
	v_pk_mul_f32 v[6:7], v[6:7], v[14:15]
	v_pk_mul_f32 v[0:1], v[0:1], v[8:9]
	v_pk_mul_f32 v[2:3], v[2:3], v[10:11]
	v_pk_fma_f32 v[160:161], v[160:161], v[252:253], v[252:253]
	v_pk_fma_f32 v[162:163], v[162:163], v[252:253], v[252:253]
	v_pk_fma_f32 v[164:165], v[164:165], v[252:253], v[252:253]
	v_pk_fma_f32 v[166:167], v[166:167], v[252:253], v[252:253]
	v_rcp_f32_e32 v160, v160
	v_rcp_f32_e32 v161, v161
	v_rcp_f32_e32 v162, v162
	v_rcp_f32_e32 v163, v163
	v_rcp_f32_e32 v164, v164
	v_rcp_f32_e32 v165, v165
	v_rcp_f32_e32 v166, v166
	v_rcp_f32_e32 v167, v167
	v_add_u32_e32 v170, 0x134000, v246
	v_pk_mul_f32 v[4:5], v[4:5], v[160:161]
	v_pk_mul_f32 v[6:7], v[6:7], v[162:163]
	v_pk_mul_f32 v[0:1], v[0:1], v[164:165]
	v_pk_mul_f32 v[2:3], v[2:3], v[166:167]
	v_med3_f32 v4, v4, s51, v144
	v_med3_f32 v5, v5, s51, v144
	v_med3_f32 v6, v6, s51, v144
	v_med3_f32 v7, v7, s51, v144
	v_med3_f32 v0, v0, s51, v144
	v_med3_f32 v1, v1, s51, v144
	v_med3_f32 v2, v2, s51, v144
	v_med3_f32 v3, v3, s51, v144
	v_cvt_pk_fp8_f32 v168, v4, v5
	v_cvt_pk_fp8_f32 v169, v0, v1
	v_cvt_pk_fp8_f32 v168, v6, v7 op_sel:[0,0,1]
	v_cvt_pk_fp8_f32 v169, v2, v3 op_sel:[0,0,1]
	s_nop 0
	global_store_dwordx2 v170, v[168:169], s[10:11]
	s_and_b64 vcc, exec, s[4:5]
	s_mov_b64 s[4:5], -1
	s_cbranch_vccnz .LBB0_1403
	s_andn2_b64 vcc, exec, s[8:9]
	s_cbranch_vccnz .LBB0_1402
	s_branch .LBB0_1402
